# speedup vs baseline: 1.0058x; 1.0020x over previous
.Lg1_noX:
	v_permlane16_swap_b32_e32 v158, v160
	v_permlane16_swap_b32_e32 v159, v161
	global_store_dwordx4 v228, v[158:161], s[58:59] offset:128 nt
	v_exp_f32_e32 v130, v90
	v_exp_f32_e32 v131, v91
	v_exp_f32_e32 v132, v92
	v_exp_f32_e32 v133, v93
	v_exp_f32_e32 v142, v42
	v_exp_f32_e32 v143, v43
	v_exp_f32_e32 v144, v44
	v_exp_f32_e32 v145, v45
	v_exp_f32_e32 v176, v126
	v_exp_f32_e32 v177, v127
	v_exp_f32_e32 v178, v128
	v_exp_f32_e32 v179, v129
	v_exp_f32_e32 v232, v58
	v_exp_f32_e32 v233, v59
	v_exp_f32_e32 v234, v60
	v_exp_f32_e32 v235, v61
	v_pk_fma_f32 v[130:131], v[130:131], -0.5, -0.5 op_sel_hi:[1,0,0]
	v_pk_fma_f32 v[132:133], v[132:133], -0.5, -0.5 op_sel_hi:[1,0,0]
	v_pk_fma_f32 v[142:143], v[142:143], -0.5, -0.5 op_sel_hi:[1,0,0]
	v_pk_fma_f32 v[144:145], v[144:145], -0.5, -0.5 op_sel_hi:[1,0,0]
	v_pk_fma_f32 v[176:177], v[176:177], -0.5, -0.5 op_sel_hi:[1,0,0]
	v_pk_fma_f32 v[178:179], v[178:179], -0.5, -0.5 op_sel_hi:[1,0,0]
	v_pk_fma_f32 v[232:233], v[232:233], -0.5, -0.5 op_sel_hi:[1,0,0]
	v_pk_fma_f32 v[234:235], v[234:235], -0.5, -0.5 op_sel_hi:[1,0,0]
	v_pk_mul_f32 v[134:135], v[130:131], v[132:133]
	v_pk_mul_f32 v[146:147], v[142:143], v[144:145]
	v_pk_mul_f32 v[180:181], v[176:177], v[178:179]
	v_pk_mul_f32 v[236:237], v[232:233], v[234:235]
	v_mul_f32_e32 v138, v134, v135
	v_mul_f32_e32 v150, v146, v147
	v_mul_f32_e32 v184, v180, v181
	v_mul_f32_e32 v240, v236, v237
	v_rcp_f32_e32 v138, v138
	v_rcp_f32_e32 v150, v150
	v_rcp_f32_e32 v184, v184
	v_rcp_f32_e32 v240, v240
	v_pk_add_f32 v[164:165], v[164:165], v[90:91]
	v_pk_add_f32 v[164:165], v[164:165], v[92:93]
	v_pk_add_f32 v[164:165], v[164:165], v[42:43]
	v_pk_add_f32 v[164:165], v[164:165], v[44:45]
	v_pk_add_f32 v[164:165], v[164:165], v[126:127]
	v_pk_add_f32 v[164:165], v[164:165], v[128:129]
	v_pk_add_f32 v[164:165], v[164:165], v[58:59]
	v_pk_add_f32 v[164:165], v[164:165], v[60:61]
	v_pk_mul_f32 v[174:175], v[134:135], v[146:147]
	v_pk_mul_f32 v[174:175], v[174:175], v[180:181]
	v_pk_mul_f32 v[174:175], v[174:175], v[236:237]
	v_pk_mul_f32 v[136:137], v[138:139], v[134:135] op_sel:[0,1] op_sel_hi:[0,0]
	v_pk_mul_f32 v[148:149], v[150:151], v[146:147] op_sel:[0,1] op_sel_hi:[0,0]
	v_pk_mul_f32 v[182:183], v[184:185], v[180:181] op_sel:[0,1] op_sel_hi:[0,0]
	v_pk_mul_f32 v[238:239], v[240:241], v[236:237] op_sel:[0,1] op_sel_hi:[0,0]
	v_pk_fma_f32 v[138:139], v[136:137], v[132:133], 1.0 op_sel_hi:[1,1,0]
	v_pk_fma_f32 v[140:141], v[136:137], v[130:131], 1.0 op_sel_hi:[1,1,0]
	v_pk_fma_f32 v[150:151], v[148:149], v[144:145], 1.0 op_sel_hi:[1,1,0]
	v_pk_fma_f32 v[152:153], v[148:149], v[142:143], 1.0 op_sel_hi:[1,1,0]
	v_pk_fma_f32 v[184:185], v[182:183], v[178:179], 1.0 op_sel_hi:[1,1,0]
	v_pk_fma_f32 v[186:187], v[182:183], v[176:177], 1.0 op_sel_hi:[1,1,0]
	v_pk_fma_f32 v[240:241], v[238:239], v[234:235], 1.0 op_sel_hi:[1,1,0]
	v_pk_fma_f32 v[242:243], v[238:239], v[232:233], 1.0 op_sel_hi:[1,1,0]
	v_cvt_pk_bf16_f32 v154, v138, v139
	v_cvt_pk_bf16_f32 v155, v140, v141
	v_cvt_pk_bf16_f32 v156, v150, v151
	v_cvt_pk_bf16_f32 v157, v152, v153
	v_cvt_pk_bf16_f32 v158, v184, v185
	v_cvt_pk_bf16_f32 v159, v186, v187
	v_cvt_pk_bf16_f32 v160, v240, v241
	v_cvt_pk_bf16_f32 v161, v242, v243
	ds_read_b128 v[90:93], v172 offset:512
	ds_read_b128 v[42:45], v172 offset:576
	ds_read_b128 v[126:129], v172 offset:640
	ds_read_b128 v[58:61], v172 offset:704
	v_permlane16_swap_b32_e32 v154, v156
	v_permlane16_swap_b32_e32 v155, v157
	global_store_dwordx4 v228, v[154:157], s[62:63] nt
	v_permlane16_swap_b32_e32 v158, v160
	v_permlane16_swap_b32_e32 v159, v161
	global_store_dwordx4 v228, v[158:161], s[62:63] offset:128 nt
	v_log_f32_e32 v166, v162
	v_log_f32_e32 v167, v163
	v_log_f32_e32 v170, v174
	v_log_f32_e32 v171, v175
	v_add_f32_e32 v168, v164, v165
	v_mul_f32_e32 v168, 0xbeb17218, v168
	v_add_f32_e32 v166, v166, v167
	v_add_f32_e32 v170, v170, v171
	v_add_f32_e32 v166, v166, v170
	v_fmac_f32_e32 v168, 0x3f317218, v166
	v_mov_b32_e32 v169, v168
	s_nop 1
	v_permlane16_swap_b32_e32 v168, v169
	v_add_f32_e32 v168, v168, v169
	v_mov_b32_e32 v169, v168
	s_nop 1
	v_permlane32_swap_b32_e32 v168, v169
	v_add_f32_e32 v168, v168, v169
	s_mov_b64 exec, s[0:1]
	global_store_dword v229, v168, s[66:67]
	s_mov_b64 exec, -1
	v_exp_f32_e32 v130, v110
	v_exp_f32_e32 v131, v111
	v_exp_f32_e32 v132, v112
	v_exp_f32_e32 v133, v113
	v_exp_f32_e32 v142, v74
	v_exp_f32_e32 v143, v75
	v_exp_f32_e32 v144, v76
	v_exp_f32_e32 v145, v77
	v_exp_f32_e32 v176, v102
	v_exp_f32_e32 v177, v103
	v_exp_f32_e32 v178, v104
	v_exp_f32_e32 v179, v105
	v_exp_f32_e32 v232, v66
	v_exp_f32_e32 v233, v67
	v_exp_f32_e32 v234, v68
	v_exp_f32_e32 v235, v69
	v_pk_fma_f32 v[130:131], v[130:131], -0.5, -0.5 op_sel_hi:[1,0,0]
	v_pk_fma_f32 v[132:133], v[132:133], -0.5, -0.5 op_sel_hi:[1,0,0]
	v_pk_fma_f32 v[142:143], v[142:143], -0.5, -0.5 op_sel_hi:[1,0,0]
	v_pk_fma_f32 v[144:145], v[144:145], -0.5, -0.5 op_sel_hi:[1,0,0]
	v_pk_fma_f32 v[176:177], v[176:177], -0.5, -0.5 op_sel_hi:[1,0,0]
	v_pk_fma_f32 v[178:179], v[178:179], -0.5, -0.5 op_sel_hi:[1,0,0]
	v_pk_fma_f32 v[232:233], v[232:233], -0.5, -0.5 op_sel_hi:[1,0,0]
	v_pk_fma_f32 v[234:235], v[234:235], -0.5, -0.5 op_sel_hi:[1,0,0]
	v_pk_mul_f32 v[134:135], v[130:131], v[132:133]
	v_pk_mul_f32 v[146:147], v[142:143], v[144:145]
	v_pk_mul_f32 v[180:181], v[176:177], v[178:179]
	v_pk_mul_f32 v[236:237], v[232:233], v[234:235]
	v_mul_f32_e32 v138, v134, v135
	v_mul_f32_e32 v150, v146, v147
	v_mul_f32_e32 v184, v180, v181
	v_mul_f32_e32 v240, v236, v237
	v_rcp_f32_e32 v138, v138
	v_rcp_f32_e32 v150, v150
	v_rcp_f32_e32 v184, v184
	v_rcp_f32_e32 v240, v240
	v_pk_add_f32 v[164:165], v[110:111], v[112:113]
	v_pk_add_f32 v[164:165], v[164:165], v[74:75]
	v_pk_add_f32 v[164:165], v[164:165], v[76:77]
	v_pk_add_f32 v[164:165], v[164:165], v[102:103]
	v_pk_add_f32 v[164:165], v[164:165], v[104:105]
	v_pk_add_f32 v[164:165], v[164:165], v[66:67]
	v_pk_add_f32 v[164:165], v[164:165], v[68:69]
	v_pk_mul_f32 v[162:163], v[134:135], v[146:147]
	v_pk_mul_f32 v[162:163], v[162:163], v[180:181]
	v_pk_mul_f32 v[162:163], v[162:163], v[236:237]
	v_pk_mul_f32 v[136:137], v[138:139], v[134:135] op_sel:[0,1] op_sel_hi:[0,0]
	v_pk_mul_f32 v[148:149], v[150:151], v[146:147] op_sel:[0,1] op_sel_hi:[0,0]
	v_pk_mul_f32 v[182:183], v[184:185], v[180:181] op_sel:[0,1] op_sel_hi:[0,0]
	v_pk_mul_f32 v[238:239], v[240:241], v[236:237] op_sel:[0,1] op_sel_hi:[0,0]
	v_pk_fma_f32 v[138:139], v[136:137], v[132:133], 1.0 op_sel_hi:[1,1,0]
	v_pk_fma_f32 v[140:141], v[136:137], v[130:131], 1.0 op_sel_hi:[1,1,0]
	v_pk_fma_f32 v[150:151], v[148:149], v[144:145], 1.0 op_sel_hi:[1,1,0]
	v_pk_fma_f32 v[152:153], v[148:149], v[142:143], 1.0 op_sel_hi:[1,1,0]
	v_pk_fma_f32 v[184:185], v[182:183], v[178:179], 1.0 op_sel_hi:[1,1,0]
	v_pk_fma_f32 v[186:187], v[182:183], v[176:177], 1.0 op_sel_hi:[1,1,0]
	v_pk_fma_f32 v[240:241], v[238:239], v[234:235], 1.0 op_sel_hi:[1,1,0]
	v_pk_fma_f32 v[242:243], v[238:239], v[232:233], 1.0 op_sel_hi:[1,1,0]
	v_cvt_pk_bf16_f32 v154, v138, v139
	v_cvt_pk_bf16_f32 v155, v140, v141
	v_cvt_pk_bf16_f32 v156, v150, v151
	v_cvt_pk_bf16_f32 v157, v152, v153
	v_cvt_pk_bf16_f32 v158, v184, v185
	v_cvt_pk_bf16_f32 v159, v186, v187
	v_cvt_pk_bf16_f32 v160, v240, v241
	v_cvt_pk_bf16_f32 v161, v242, v243
	ds_read_b128 v[110:113], v172
	ds_read_b128 v[74:77], v172 offset:64
	ds_read_b128 v[102:105], v172 offset:128
	ds_read_b128 v[66:69], v172 offset:192
	v_permlane16_swap_b32_e32 v154, v156
	v_permlane16_swap_b32_e32 v155, v157
	global_store_dwordx4 v228, v[154:157], s[58:59] offset:2048 nt
	v_permlane16_swap_b32_e32 v158, v160
	v_permlane16_swap_b32_e32 v159, v161
	global_store_dwordx4 v228, v[158:161], s[58:59] offset:2176 nt
	v_exp_f32_e32 v130, v86
	v_exp_f32_e32 v131, v87
	v_exp_f32_e32 v132, v88
	v_exp_f32_e32 v133, v89
	v_exp_f32_e32 v142, v38
	v_exp_f32_e32 v143, v39
	v_exp_f32_e32 v144, v40
	v_exp_f32_e32 v145, v41
	v_exp_f32_e32 v176, v122
	v_exp_f32_e32 v177, v123
	v_exp_f32_e32 v178, v124
	v_exp_f32_e32 v179, v125
	v_exp_f32_e32 v232, v50
	v_exp_f32_e32 v233, v51
	v_exp_f32_e32 v234, v52
	v_exp_f32_e32 v235, v53
	v_pk_fma_f32 v[130:131], v[130:131], -0.5, -0.5 op_sel_hi:[1,0,0]
	v_pk_fma_f32 v[132:133], v[132:133], -0.5, -0.5 op_sel_hi:[1,0,0]
	v_pk_fma_f32 v[142:143], v[142:143], -0.5, -0.5 op_sel_hi:[1,0,0]
	v_pk_fma_f32 v[144:145], v[144:145], -0.5, -0.5 op_sel_hi:[1,0,0]
	v_pk_fma_f32 v[176:177], v[176:177], -0.5, -0.5 op_sel_hi:[1,0,0]
	v_pk_fma_f32 v[178:179], v[178:179], -0.5, -0.5 op_sel_hi:[1,0,0]
	v_pk_fma_f32 v[232:233], v[232:233], -0.5, -0.5 op_sel_hi:[1,0,0]
	v_pk_fma_f32 v[234:235], v[234:235], -0.5, -0.5 op_sel_hi:[1,0,0]
	v_pk_mul_f32 v[134:135], v[130:131], v[132:133]
	v_pk_mul_f32 v[146:147], v[142:143], v[144:145]
	v_pk_mul_f32 v[180:181], v[176:177], v[178:179]
	v_pk_mul_f32 v[236:237], v[232:233], v[234:235]
	v_mul_f32_e32 v138, v134, v135
	v_mul_f32_e32 v150, v146, v147
	v_mul_f32_e32 v184, v180, v181
	v_mul_f32_e32 v240, v236, v237
	v_rcp_f32_e32 v138, v138
	v_rcp_f32_e32 v150, v150
	v_rcp_f32_e32 v184, v184
	v_rcp_f32_e32 v240, v240
	v_pk_add_f32 v[164:165], v[164:165], v[86:87]
	v_pk_add_f32 v[164:165], v[164:165], v[88:89]
	v_pk_add_f32 v[164:165], v[164:165], v[38:39]
	v_pk_add_f32 v[164:165], v[164:165], v[40:41]
	v_pk_add_f32 v[164:165], v[164:165], v[122:123]
	v_pk_add_f32 v[164:165], v[164:165], v[124:125]
	v_pk_add_f32 v[164:165], v[164:165], v[50:51]
	v_pk_add_f32 v[164:165], v[164:165], v[52:53]
	v_pk_mul_f32 v[174:175], v[134:135], v[146:147]
	v_pk_mul_f32 v[174:175], v[174:175], v[180:181]
	v_pk_mul_f32 v[174:175], v[174:175], v[236:237]
	v_pk_mul_f32 v[136:137], v[138:139], v[134:135] op_sel:[0,1] op_sel_hi:[0,0]
	v_pk_mul_f32 v[148:149], v[150:151], v[146:147] op_sel:[0,1] op_sel_hi:[0,0]
	v_pk_mul_f32 v[182:183], v[184:185], v[180:181] op_sel:[0,1] op_sel_hi:[0,0]
	v_pk_mul_f32 v[238:239], v[240:241], v[236:237] op_sel:[0,1] op_sel_hi:[0,0]
	v_pk_fma_f32 v[138:139], v[136:137], v[132:133], 1.0 op_sel_hi:[1,1,0]
	v_pk_fma_f32 v[140:141], v[136:137], v[130:131], 1.0 op_sel_hi:[1,1,0]
	v_pk_fma_f32 v[150:151], v[148:149], v[144:145], 1.0 op_sel_hi:[1,1,0]
	v_pk_fma_f32 v[152:153], v[148:149], v[142:143], 1.0 op_sel_hi:[1,1,0]
	v_pk_fma_f32 v[184:185], v[182:183], v[178:179], 1.0 op_sel_hi:[1,1,0]
	v_pk_fma_f32 v[186:187], v[182:183], v[176:177], 1.0 op_sel_hi:[1,1,0]
	v_pk_fma_f32 v[240:241], v[238:239], v[234:235], 1.0 op_sel_hi:[1,1,0]
	v_pk_fma_f32 v[242:243], v[238:239], v[232:233], 1.0 op_sel_hi:[1,1,0]
	v_cvt_pk_bf16_f32 v154, v138, v139
	v_cvt_pk_bf16_f32 v155, v140, v141
	v_cvt_pk_bf16_f32 v156, v150, v151
	v_cvt_pk_bf16_f32 v157, v152, v153
	v_cvt_pk_bf16_f32 v158, v184, v185
	v_cvt_pk_bf16_f32 v159, v186, v187
	v_cvt_pk_bf16_f32 v160, v240, v241
	v_cvt_pk_bf16_f32 v161, v242, v243
	ds_read_b128 v[86:89], v172 offset:512
	ds_read_b128 v[38:41], v172 offset:576
	ds_read_b128 v[122:125], v172 offset:640
	ds_read_b128 v[50:53], v172 offset:704
	v_permlane16_swap_b32_e32 v154, v156
	v_permlane16_swap_b32_e32 v155, v157
	global_store_dwordx4 v228, v[154:157], s[62:63] offset:2048 nt
	v_permlane16_swap_b32_e32 v158, v160
	v_permlane16_swap_b32_e32 v159, v161
	global_store_dwordx4 v228, v[158:161], s[62:63] offset:2176 nt
	v_log_f32_e32 v166, v162
	v_log_f32_e32 v167, v163
	v_log_f32_e32 v170, v174
	v_log_f32_e32 v171, v175
	v_add_f32_e32 v168, v164, v165
	v_mul_f32_e32 v168, 0xbeb17218, v168
	v_add_f32_e32 v166, v166, v167
	v_add_f32_e32 v170, v170, v171
	v_add_f32_e32 v166, v166, v170
	v_fmac_f32_e32 v168, 0x3f317218, v166
	v_mov_b32_e32 v169, v168
	s_nop 1
	v_permlane16_swap_b32_e32 v168, v169
	v_add_f32_e32 v168, v168, v169
	v_mov_b32_e32 v169, v168
	s_nop 1
	v_permlane32_swap_b32_e32 v168, v169
	v_add_f32_e32 v168, v168, v169
	s_mov_b64 exec, s[0:1]
	global_store_dword v229, v168, s[66:67] offset:64
	s_mov_b64 exec, -1
	v_exp_f32_e32 v130, v98
	v_exp_f32_e32 v131, v99
	v_exp_f32_e32 v132, v100
	v_exp_f32_e32 v133, v101
	v_exp_f32_e32 v142, v62
	v_exp_f32_e32 v143, v63
	v_exp_f32_e32 v144, v64
	v_exp_f32_e32 v145, v65
	v_exp_f32_e32 v176, v94
	v_exp_f32_e32 v177, v95
	v_exp_f32_e32 v178, v96
	v_exp_f32_e32 v179, v97
	v_exp_f32_e32 v232, v54
	v_exp_f32_e32 v233, v55
	v_exp_f32_e32 v234, v56
	v_exp_f32_e32 v235, v57
	v_pk_fma_f32 v[130:131], v[130:131], -0.5, -0.5 op_sel_hi:[1,0,0]
	v_pk_fma_f32 v[132:133], v[132:133], -0.5, -0.5 op_sel_hi:[1,0,0]
	v_pk_fma_f32 v[142:143], v[142:143], -0.5, -0.5 op_sel_hi:[1,0,0]
	v_pk_fma_f32 v[144:145], v[144:145], -0.5, -0.5 op_sel_hi:[1,0,0]
	v_pk_fma_f32 v[176:177], v[176:177], -0.5, -0.5 op_sel_hi:[1,0,0]
	v_pk_fma_f32 v[178:179], v[178:179], -0.5, -0.5 op_sel_hi:[1,0,0]
	v_pk_fma_f32 v[232:233], v[232:233], -0.5, -0.5 op_sel_hi:[1,0,0]
	v_pk_fma_f32 v[234:235], v[234:235], -0.5, -0.5 op_sel_hi:[1,0,0]
	v_pk_mul_f32 v[134:135], v[130:131], v[132:133]
	v_pk_mul_f32 v[146:147], v[142:143], v[144:145]
	v_pk_mul_f32 v[180:181], v[176:177], v[178:179]
	v_pk_mul_f32 v[236:237], v[232:233], v[234:235]
	v_mul_f32_e32 v138, v134, v135
	v_mul_f32_e32 v150, v146, v147
	v_mul_f32_e32 v184, v180, v181
	v_mul_f32_e32 v240, v236, v237
	v_rcp_f32_e32 v138, v138
	v_rcp_f32_e32 v150, v150
	v_rcp_f32_e32 v184, v184
	v_rcp_f32_e32 v240, v240
	v_pk_add_f32 v[164:165], v[98:99], v[100:101]
	v_pk_add_f32 v[164:165], v[164:165], v[62:63]
	v_pk_add_f32 v[164:165], v[164:165], v[64:65]
	v_pk_add_f32 v[164:165], v[164:165], v[94:95]
	v_pk_add_f32 v[164:165], v[164:165], v[96:97]
	v_pk_add_f32 v[164:165], v[164:165], v[54:55]
	v_pk_add_f32 v[164:165], v[164:165], v[56:57]
	v_pk_mul_f32 v[162:163], v[134:135], v[146:147]
	v_pk_mul_f32 v[162:163], v[162:163], v[180:181]
	v_pk_mul_f32 v[162:163], v[162:163], v[236:237]
	v_pk_mul_f32 v[136:137], v[138:139], v[134:135] op_sel:[0,1] op_sel_hi:[0,0]
	v_pk_mul_f32 v[148:149], v[150:151], v[146:147] op_sel:[0,1] op_sel_hi:[0,0]
	v_pk_mul_f32 v[182:183], v[184:185], v[180:181] op_sel:[0,1] op_sel_hi:[0,0]
	v_pk_mul_f32 v[238:239], v[240:241], v[236:237] op_sel:[0,1] op_sel_hi:[0,0]
	v_pk_fma_f32 v[138:139], v[136:137], v[132:133], 1.0 op_sel_hi:[1,1,0]
	v_pk_fma_f32 v[140:141], v[136:137], v[130:131], 1.0 op_sel_hi:[1,1,0]
	v_pk_fma_f32 v[150:151], v[148:149], v[144:145], 1.0 op_sel_hi:[1,1,0]
	v_pk_fma_f32 v[152:153], v[148:149], v[142:143], 1.0 op_sel_hi:[1,1,0]
	v_pk_fma_f32 v[184:185], v[182:183], v[178:179], 1.0 op_sel_hi:[1,1,0]
	v_pk_fma_f32 v[186:187], v[182:183], v[176:177], 1.0 op_sel_hi:[1,1,0]
	v_pk_fma_f32 v[240:241], v[238:239], v[234:235], 1.0 op_sel_hi:[1,1,0]
	v_pk_fma_f32 v[242:243], v[238:239], v[232:233], 1.0 op_sel_hi:[1,1,0]
	v_cvt_pk_bf16_f32 v154, v138, v139
	v_cvt_pk_bf16_f32 v155, v140, v141
	v_cvt_pk_bf16_f32 v156, v150, v151
	v_cvt_pk_bf16_f32 v157, v152, v153
	v_cvt_pk_bf16_f32 v158, v184, v185
	v_cvt_pk_bf16_f32 v159, v186, v187
	v_cvt_pk_bf16_f32 v160, v240, v241
	v_cvt_pk_bf16_f32 v161, v242, v243
	ds_read_b128 v[98:101], v172
	ds_read_b128 v[62:65], v172 offset:64
	ds_read_b128 v[94:97], v172 offset:128
	ds_read_b128 v[54:57], v172 offset:192
	v_permlane16_swap_b32_e32 v154, v156
	v_permlane16_swap_b32_e32 v155, v157
	global_store_dwordx4 v228, v[154:157], s[60:61] nt
	v_permlane16_swap_b32_e32 v158, v160
	v_permlane16_swap_b32_e32 v159, v161
	global_store_dwordx4 v228, v[158:161], s[60:61] offset:128 nt
	v_exp_f32_e32 v130, v82
	v_exp_f32_e32 v131, v83
	v_exp_f32_e32 v132, v84
	v_exp_f32_e32 v133, v85
	v_exp_f32_e32 v142, v34
	v_exp_f32_e32 v143, v35
	v_exp_f32_e32 v144, v36
	v_exp_f32_e32 v145, v37
	v_exp_f32_e32 v176, v118
	v_exp_f32_e32 v177, v119
	v_exp_f32_e32 v178, v120
	v_exp_f32_e32 v179, v121
	v_exp_f32_e32 v232, v46
	v_exp_f32_e32 v233, v47
	v_exp_f32_e32 v234, v48
	v_exp_f32_e32 v235, v49
	v_pk_fma_f32 v[130:131], v[130:131], -0.5, -0.5 op_sel_hi:[1,0,0]
	v_pk_fma_f32 v[132:133], v[132:133], -0.5, -0.5 op_sel_hi:[1,0,0]
	v_pk_fma_f32 v[142:143], v[142:143], -0.5, -0.5 op_sel_hi:[1,0,0]
	v_pk_fma_f32 v[144:145], v[144:145], -0.5, -0.5 op_sel_hi:[1,0,0]
	v_pk_fma_f32 v[176:177], v[176:177], -0.5, -0.5 op_sel_hi:[1,0,0]
	v_pk_fma_f32 v[178:179], v[178:179], -0.5, -0.5 op_sel_hi:[1,0,0]
	v_pk_fma_f32 v[232:233], v[232:233], -0.5, -0.5 op_sel_hi:[1,0,0]
	v_pk_fma_f32 v[234:235], v[234:235], -0.5, -0.5 op_sel_hi:[1,0,0]
	v_pk_mul_f32 v[134:135], v[130:131], v[132:133]
	v_pk_mul_f32 v[146:147], v[142:143], v[144:145]
	v_pk_mul_f32 v[180:181], v[176:177], v[178:179]
	v_pk_mul_f32 v[236:237], v[232:233], v[234:235]
	v_mul_f32_e32 v138, v134, v135
	v_mul_f32_e32 v150, v146, v147
	v_mul_f32_e32 v184, v180, v181
	v_mul_f32_e32 v240, v236, v237
	v_rcp_f32_e32 v138, v138
	v_rcp_f32_e32 v150, v150
	v_rcp_f32_e32 v184, v184
	v_rcp_f32_e32 v240, v240
	v_pk_add_f32 v[164:165], v[164:165], v[82:83]
	v_pk_add_f32 v[164:165], v[164:165], v[84:85]
	v_pk_add_f32 v[164:165], v[164:165], v[34:35]
	v_pk_add_f32 v[164:165], v[164:165], v[36:37]
	v_pk_add_f32 v[164:165], v[164:165], v[118:119]
	v_pk_add_f32 v[164:165], v[164:165], v[120:121]
	v_pk_add_f32 v[164:165], v[164:165], v[46:47]
	v_pk_add_f32 v[164:165], v[164:165], v[48:49]
	v_pk_mul_f32 v[174:175], v[134:135], v[146:147]
	v_pk_mul_f32 v[174:175], v[174:175], v[180:181]
	v_pk_mul_f32 v[174:175], v[174:175], v[236:237]
	v_pk_mul_f32 v[136:137], v[138:139], v[134:135] op_sel:[0,1] op_sel_hi:[0,0]
	v_pk_mul_f32 v[148:149], v[150:151], v[146:147] op_sel:[0,1] op_sel_hi:[0,0]
	v_pk_mul_f32 v[182:183], v[184:185], v[180:181] op_sel:[0,1] op_sel_hi:[0,0]
	v_pk_mul_f32 v[238:239], v[240:241], v[236:237] op_sel:[0,1] op_sel_hi:[0,0]
	v_pk_fma_f32 v[138:139], v[136:137], v[132:133], 1.0 op_sel_hi:[1,1,0]
	v_pk_fma_f32 v[140:141], v[136:137], v[130:131], 1.0 op_sel_hi:[1,1,0]
	v_pk_fma_f32 v[150:151], v[148:149], v[144:145], 1.0 op_sel_hi:[1,1,0]
	v_pk_fma_f32 v[152:153], v[148:149], v[142:143], 1.0 op_sel_hi:[1,1,0]
	v_pk_fma_f32 v[184:185], v[182:183], v[178:179], 1.0 op_sel_hi:[1,1,0]
	v_pk_fma_f32 v[186:187], v[182:183], v[176:177], 1.0 op_sel_hi:[1,1,0]
	v_pk_fma_f32 v[240:241], v[238:239], v[234:235], 1.0 op_sel_hi:[1,1,0]
	v_pk_fma_f32 v[242:243], v[238:239], v[232:233], 1.0 op_sel_hi:[1,1,0]
	v_cvt_pk_bf16_f32 v154, v138, v139
	v_cvt_pk_bf16_f32 v155, v140, v141
	v_cvt_pk_bf16_f32 v156, v150, v151
	v_cvt_pk_bf16_f32 v157, v152, v153
	v_cvt_pk_bf16_f32 v158, v184, v185
	v_cvt_pk_bf16_f32 v159, v186, v187
	v_cvt_pk_bf16_f32 v160, v240, v241
	v_cvt_pk_bf16_f32 v161, v242, v243
	ds_read_b128 v[82:85], v172 offset:512
	ds_read_b128 v[34:37], v172 offset:576
	ds_read_b128 v[118:121], v172 offset:640
	ds_read_b128 v[46:49], v172 offset:704
	v_permlane16_swap_b32_e32 v154, v156
	v_permlane16_swap_b32_e32 v155, v157
	global_store_dwordx4 v228, v[154:157], s[64:65] nt
	v_permlane16_swap_b32_e32 v158, v160
	v_permlane16_swap_b32_e32 v159, v161
	global_store_dwordx4 v228, v[158:161], s[64:65] offset:128 nt
	v_log_f32_e32 v166, v162
	v_log_f32_e32 v167, v163
	v_log_f32_e32 v170, v174
	v_log_f32_e32 v171, v175
	v_add_f32_e32 v168, v164, v165
	v_mul_f32_e32 v168, 0xbeb17218, v168
	v_add_f32_e32 v166, v166, v167
	v_add_f32_e32 v170, v170, v171
	v_add_f32_e32 v166, v166, v170
	v_fmac_f32_e32 v168, 0x3f317218, v166
	v_mov_b32_e32 v169, v168
	s_nop 1
	v_permlane16_swap_b32_e32 v168, v169
	v_add_f32_e32 v168, v168, v169
	v_mov_b32_e32 v169, v168
	s_nop 1
	v_permlane32_swap_b32_e32 v168, v169
	v_add_f32_e32 v168, v168, v169
	s_mov_b64 exec, s[0:1]
	global_store_dword v229, v168, s[66:67] offset:512
	s_mov_b64 exec, -1
	v_exp_f32_e32 v130, v18
	v_exp_f32_e32 v131, v19
	v_exp_f32_e32 v132, v20
	v_exp_f32_e32 v133, v21
	v_exp_f32_e32 v142, v2
	v_exp_f32_e32 v143, v3
	v_exp_f32_e32 v144, v4
	v_exp_f32_e32 v145, v5
	v_exp_f32_e32 v176, v26
	v_exp_f32_e32 v177, v27
	v_exp_f32_e32 v178, v28
	v_exp_f32_e32 v179, v29
	v_exp_f32_e32 v232, v10
	v_exp_f32_e32 v233, v11
	v_exp_f32_e32 v234, v12
	v_exp_f32_e32 v235, v13
	v_pk_fma_f32 v[130:131], v[130:131], -0.5, -0.5 op_sel_hi:[1,0,0]
	v_pk_fma_f32 v[132:133], v[132:133], -0.5, -0.5 op_sel_hi:[1,0,0]
	v_pk_fma_f32 v[142:143], v[142:143], -0.5, -0.5 op_sel_hi:[1,0,0]
	v_pk_fma_f32 v[144:145], v[144:145], -0.5, -0.5 op_sel_hi:[1,0,0]
	v_pk_fma_f32 v[176:177], v[176:177], -0.5, -0.5 op_sel_hi:[1,0,0]
	v_pk_fma_f32 v[178:179], v[178:179], -0.5, -0.5 op_sel_hi:[1,0,0]
	v_pk_fma_f32 v[232:233], v[232:233], -0.5, -0.5 op_sel_hi:[1,0,0]
	v_pk_fma_f32 v[234:235], v[234:235], -0.5, -0.5 op_sel_hi:[1,0,0]
	v_pk_mul_f32 v[134:135], v[130:131], v[132:133]
	v_pk_mul_f32 v[146:147], v[142:143], v[144:145]
	v_pk_mul_f32 v[180:181], v[176:177], v[178:179]
	v_pk_mul_f32 v[236:237], v[232:233], v[234:235]
	v_mul_f32_e32 v138, v134, v135
	v_mul_f32_e32 v150, v146, v147
	v_mul_f32_e32 v184, v180, v181
	v_mul_f32_e32 v240, v236, v237
	v_rcp_f32_e32 v138, v138
	v_rcp_f32_e32 v150, v150
	v_rcp_f32_e32 v184, v184
	v_rcp_f32_e32 v240, v240
	v_pk_add_f32 v[164:165], v[18:19], v[20:21]
	v_pk_add_f32 v[164:165], v[164:165], v[2:3]
	v_pk_add_f32 v[164:165], v[164:165], v[4:5]
	v_pk_add_f32 v[164:165], v[164:165], v[26:27]
	v_pk_add_f32 v[164:165], v[164:165], v[28:29]
	v_pk_add_f32 v[164:165], v[164:165], v[10:11]
	v_pk_add_f32 v[164:165], v[164:165], v[12:13]
	v_pk_mul_f32 v[162:163], v[134:135], v[146:147]
	v_pk_mul_f32 v[162:163], v[162:163], v[180:181]
	v_pk_mul_f32 v[162:163], v[162:163], v[236:237]
	v_pk_mul_f32 v[136:137], v[138:139], v[134:135] op_sel:[0,1] op_sel_hi:[0,0]
	v_pk_mul_f32 v[148:149], v[150:151], v[146:147] op_sel:[0,1] op_sel_hi:[0,0]
	v_pk_mul_f32 v[182:183], v[184:185], v[180:181] op_sel:[0,1] op_sel_hi:[0,0]
	v_pk_mul_f32 v[238:239], v[240:241], v[236:237] op_sel:[0,1] op_sel_hi:[0,0]
	v_pk_fma_f32 v[138:139], v[136:137], v[132:133], 1.0 op_sel_hi:[1,1,0]
	v_pk_fma_f32 v[140:141], v[136:137], v[130:131], 1.0 op_sel_hi:[1,1,0]
	v_pk_fma_f32 v[150:151], v[148:149], v[144:145], 1.0 op_sel_hi:[1,1,0]
	v_pk_fma_f32 v[152:153], v[148:149], v[142:143], 1.0 op_sel_hi:[1,1,0]
	v_pk_fma_f32 v[184:185], v[182:183], v[178:179], 1.0 op_sel_hi:[1,1,0]
	v_pk_fma_f32 v[186:187], v[182:183], v[176:177], 1.0 op_sel_hi:[1,1,0]
	v_pk_fma_f32 v[240:241], v[238:239], v[234:235], 1.0 op_sel_hi:[1,1,0]
	v_pk_fma_f32 v[242:243], v[238:239], v[232:233], 1.0 op_sel_hi:[1,1,0]
	v_cvt_pk_bf16_f32 v154, v138, v139
	v_cvt_pk_bf16_f32 v155, v140, v141
	v_cvt_pk_bf16_f32 v156, v150, v151
	v_cvt_pk_bf16_f32 v157, v152, v153
	v_cvt_pk_bf16_f32 v158, v184, v185
	v_cvt_pk_bf16_f32 v159, v186, v187
	v_cvt_pk_bf16_f32 v160, v240, v241
	v_cvt_pk_bf16_f32 v161, v242, v243
	ds_read_b128 v[18:21], v172
	ds_read_b128 v[2:5], v172 offset:64
	ds_read_b128 v[26:29], v172 offset:128
	ds_read_b128 v[10:13], v172 offset:192
	v_permlane16_swap_b32_e32 v154, v156
	v_permlane16_swap_b32_e32 v155, v157
	global_store_dwordx4 v228, v[154:157], s[60:61] offset:2048 nt
	v_permlane16_swap_b32_e32 v158, v160
	v_permlane16_swap_b32_e32 v159, v161
	global_store_dwordx4 v228, v[158:161], s[60:61] offset:2176 nt
	v_exp_f32_e32 v130, v22
	v_exp_f32_e32 v131, v23
	v_exp_f32_e32 v132, v24
	v_exp_f32_e32 v133, v25
	v_exp_f32_e32 v142, v6
	v_exp_f32_e32 v143, v7
	v_exp_f32_e32 v144, v8
	v_exp_f32_e32 v145, v9
	v_exp_f32_e32 v176, v30
	v_exp_f32_e32 v177, v31
	v_exp_f32_e32 v178, v32
	v_exp_f32_e32 v179, v33
	v_exp_f32_e32 v232, v14
	v_exp_f32_e32 v233, v15
	v_exp_f32_e32 v234, v16
	v_exp_f32_e32 v235, v17
	v_pk_fma_f32 v[130:131], v[130:131], -0.5, -0.5 op_sel_hi:[1,0,0]
	v_pk_fma_f32 v[132:133], v[132:133], -0.5, -0.5 op_sel_hi:[1,0,0]
	v_pk_fma_f32 v[142:143], v[142:143], -0.5, -0.5 op_sel_hi:[1,0,0]
	v_pk_fma_f32 v[144:145], v[144:145], -0.5, -0.5 op_sel_hi:[1,0,0]
	v_pk_fma_f32 v[176:177], v[176:177], -0.5, -0.5 op_sel_hi:[1,0,0]
	v_pk_fma_f32 v[178:179], v[178:179], -0.5, -0.5 op_sel_hi:[1,0,0]
	v_pk_fma_f32 v[232:233], v[232:233], -0.5, -0.5 op_sel_hi:[1,0,0]
	v_pk_fma_f32 v[234:235], v[234:235], -0.5, -0.5 op_sel_hi:[1,0,0]
	v_pk_mul_f32 v[134:135], v[130:131], v[132:133]
	v_pk_mul_f32 v[146:147], v[142:143], v[144:145]
	v_pk_mul_f32 v[180:181], v[176:177], v[178:179]
	v_pk_mul_f32 v[236:237], v[232:233], v[234:235]
	v_mul_f32_e32 v138, v134, v135
	v_mul_f32_e32 v150, v146, v147
	v_mul_f32_e32 v184, v180, v181
	v_mul_f32_e32 v240, v236, v237
	v_rcp_f32_e32 v138, v138
	v_rcp_f32_e32 v150, v150
	v_rcp_f32_e32 v184, v184
	v_rcp_f32_e32 v240, v240
	v_pk_add_f32 v[164:165], v[164:165], v[22:23]
	v_pk_add_f32 v[164:165], v[164:165], v[24:25]
	v_pk_add_f32 v[164:165], v[164:165], v[6:7]
	v_pk_add_f32 v[164:165], v[164:165], v[8:9]
	v_pk_add_f32 v[164:165], v[164:165], v[30:31]
	v_pk_add_f32 v[164:165], v[164:165], v[32:33]
	v_pk_add_f32 v[164:165], v[164:165], v[14:15]
	v_pk_add_f32 v[164:165], v[164:165], v[16:17]
	v_pk_mul_f32 v[174:175], v[134:135], v[146:147]
	v_pk_mul_f32 v[174:175], v[174:175], v[180:181]
	v_pk_mul_f32 v[174:175], v[174:175], v[236:237]
	v_pk_mul_f32 v[136:137], v[138:139], v[134:135] op_sel:[0,1] op_sel_hi:[0,0]
	v_pk_mul_f32 v[148:149], v[150:151], v[146:147] op_sel:[0,1] op_sel_hi:[0,0]
	v_pk_mul_f32 v[182:183], v[184:185], v[180:181] op_sel:[0,1] op_sel_hi:[0,0]
	v_pk_mul_f32 v[238:239], v[240:241], v[236:237] op_sel:[0,1] op_sel_hi:[0,0]
	v_pk_fma_f32 v[138:139], v[136:137], v[132:133], 1.0 op_sel_hi:[1,1,0]
	v_pk_fma_f32 v[140:141], v[136:137], v[130:131], 1.0 op_sel_hi:[1,1,0]
	v_pk_fma_f32 v[150:151], v[148:149], v[144:145], 1.0 op_sel_hi:[1,1,0]
	v_pk_fma_f32 v[152:153], v[148:149], v[142:143], 1.0 op_sel_hi:[1,1,0]
	v_pk_fma_f32 v[184:185], v[182:183], v[178:179], 1.0 op_sel_hi:[1,1,0]
	v_pk_fma_f32 v[186:187], v[182:183], v[176:177], 1.0 op_sel_hi:[1,1,0]
	v_pk_fma_f32 v[240:241], v[238:239], v[234:235], 1.0 op_sel_hi:[1,1,0]
	v_pk_fma_f32 v[242:243], v[238:239], v[232:233], 1.0 op_sel_hi:[1,1,0]
	v_cvt_pk_bf16_f32 v154, v138, v139
	v_cvt_pk_bf16_f32 v155, v140, v141
	v_cvt_pk_bf16_f32 v156, v150, v151
	v_cvt_pk_bf16_f32 v157, v152, v153
	v_cvt_pk_bf16_f32 v158, v184, v185
	v_cvt_pk_bf16_f32 v159, v186, v187
	v_cvt_pk_bf16_f32 v160, v240, v241
	v_cvt_pk_bf16_f32 v161, v242, v243
	ds_read_b128 v[22:25], v172 offset:512
	ds_read_b128 v[6:9], v172 offset:576
	ds_read_b128 v[30:33], v172 offset:640
	ds_read_b128 v[14:17], v172 offset:704
	v_permlane16_swap_b32_e32 v154, v156
	v_permlane16_swap_b32_e32 v155, v157
	global_store_dwordx4 v228, v[154:157], s[64:65] offset:2048 nt
	v_permlane16_swap_b32_e32 v158, v160
	v_permlane16_swap_b32_e32 v159, v161
	global_store_dwordx4 v228, v[158:161], s[64:65] offset:2176 nt
	v_log_f32_e32 v166, v162
	v_log_f32_e32 v167, v163
	v_log_f32_e32 v170, v174
	v_log_f32_e32 v171, v175
	v_add_f32_e32 v168, v164, v165
	v_mul_f32_e32 v168, 0xbeb17218, v168
	v_add_f32_e32 v166, v166, v167
	v_add_f32_e32 v170, v170, v171
	v_add_f32_e32 v166, v166, v170
	v_fmac_f32_e32 v168, 0x3f317218, v166
	v_mov_b32_e32 v169, v168
	s_nop 1
	v_permlane16_swap_b32_e32 v168, v169
	v_add_f32_e32 v168, v168, v169
	v_mov_b32_e32 v169, v168
	s_nop 1
	v_permlane32_swap_b32_e32 v168, v169
	v_add_f32_e32 v168, v168, v169
	s_mov_b64 exec, s[0:1]
	global_store_dword v229, v168, s[66:67] offset:576
	s_mov_b64 exec, -1
	s_bitcmp1_b32 s20, 12
	s_cbranch_scc0 .Lg1_noY
	s_barrier
.Lg1_noY:
	s_mov_b64 s[2:3], 0
	s_branch .LBB3_5
